# speedup vs baseline: 1.0074x; 1.0074x over previous
_Z6gat_k1PKfS0_S0_S0_PDF16_S1_S1_Pf:
	s_load_dwordx8 s[4:11], s[0:1], 0x0
	s_load_dwordx8 s[12:19], s[0:1], 0x20
	v_lshrrev_b32_e32 v54, 6, v0
	v_bfe_u32 v123, v0, 4, 2
	v_and_b32_e32 v120, 15, v0
	v_lshlrev_b32_e32 v120, 4, v120
	v_lshl_or_b32 v120, v54, 8, v120
	v_mov_b32_e32 v121, 0
	v_and_b32_e32 v57, 0xc0, v0
	s_lshl_b32 s3, s2, 5
	v_and_b32_e32 v1, 63, v0
	v_bfe_u32 v55, v0, 5, 1
	v_lshlrev_b32_e32 v2, 8, v57
	v_mov_b32_e32 v19, 0
	v_or_b32_e32 v4, s3, v123
	v_and_b32_e32 v56, 31, v0
	v_lshl_or_b32 v18, v55, 11, v2
	v_lshlrev_b32_e32 v20, 4, v1
	v_mov_b32_e32 v21, v19
	v_ashrrev_i32_e32 v5, 31, v4
	s_waitcnt lgkmcnt(0)
	v_lshl_add_u64 v[2:3], s[6:7], 0, v[18:19]
	v_lshlrev_b32_e32 v18, 2, v56
	s_lshl_b32 s20, s3, 10
	s_add_u32 s20, s4, s20
	s_addc_u32 s21, s5, 0
	v_lshl_or_b32 v121, v123, 10, v120
	global_load_dwordx4 v[22:25], v121, s[20:21] nt
	s_add_u32 s20, s20, 0x1000
	s_addc_u32 s21, s21, 0
	global_load_dwordx4 v[26:29], v121, s[20:21] nt
	s_add_u32 s20, s20, 0x1000
	s_addc_u32 s21, s21, 0
	global_load_dwordx4 v[30:33], v121, s[20:21] nt
	s_add_u32 s20, s20, 0x1000
	s_addc_u32 s21, s21, 0
	global_load_dwordx4 v[34:37], v121, s[20:21] nt
	s_add_u32 s20, s20, 0x1000
	s_addc_u32 s21, s21, 0
	global_load_dwordx4 v[38:41], v121, s[20:21] nt
	s_add_u32 s20, s20, 0x1000
	s_addc_u32 s21, s21, 0
	global_load_dwordx4 v[42:45], v121, s[20:21] nt
	s_add_u32 s20, s20, 0x1000
	s_addc_u32 s21, s21, 0
	global_load_dwordx4 v[46:49], v121, s[20:21] nt
	s_add_u32 s20, s20, 0x1000
	s_addc_u32 s21, s21, 0
	global_load_dwordx4 v[50:53], v121, s[20:21] nt
	s_movk_i32 s4, 0x410
	v_mad_u32_u24 v122, v123, s4, v120
	v_lshl_add_u64 v[2:3], v[2:3], 0, v[18:19]
	v_lshl_add_u64 v[2:3], v[2:3], 0, v[18:19]
	global_load_dwordx2 v[58:59], v[2:3], off
	global_load_dwordx2 v[60:61], v[2:3], off offset:256
	global_load_dwordx2 v[62:63], v[2:3], off offset:512
	global_load_dwordx2 v[64:65], v[2:3], off offset:768
	global_load_dwordx2 v[66:67], v[2:3], off offset:1024
	global_load_dwordx2 v[68:69], v[2:3], off offset:1280
	global_load_dwordx2 v[70:71], v[2:3], off offset:1536
	global_load_dwordx2 v[72:73], v[2:3], off offset:1792
	s_movk_i32 s4, 0x1000
	v_add_co_u32_e32 v4, vcc, s4, v2
	s_movk_i32 s4, 0x2000
	s_nop 0
	v_addc_co_u32_e32 v5, vcc, 0, v3, vcc
	v_add_co_u32_e32 v6, vcc, s4, v2
	s_movk_i32 s4, 0x3000
	s_nop 0
	v_addc_co_u32_e32 v7, vcc, 0, v3, vcc
	global_load_dwordx2 v[76:77], v[4:5], off offset:256
	global_load_dwordx2 v[78:79], v[4:5], off offset:512
	global_load_dwordx2 v[80:81], v[4:5], off offset:768
	global_load_dwordx2 v[82:83], v[4:5], off offset:1024
	global_load_dwordx2 v[84:85], v[4:5], off offset:1280
	global_load_dwordx2 v[86:87], v[4:5], off offset:1536
	global_load_dwordx2 v[88:89], v[4:5], off offset:1792
	global_load_dwordx2 v[74:75], v[6:7], off offset:-4096
	global_load_dwordx2 v[90:91], v[6:7], off
	global_load_dwordx2 v[92:93], v[6:7], off offset:256
	global_load_dwordx2 v[94:95], v[6:7], off offset:512
	global_load_dwordx2 v[96:97], v[6:7], off offset:768
	global_load_dwordx2 v[98:99], v[6:7], off offset:1024
	global_load_dwordx2 v[100:101], v[6:7], off offset:1280
	global_load_dwordx2 v[102:103], v[6:7], off offset:1536
	global_load_dwordx2 v[104:105], v[6:7], off offset:1792
	v_add_co_u32_e32 v2, vcc, s4, v2
	v_and_b32_e32 v1, 7, v0
	s_nop 0
	v_addc_co_u32_e32 v3, vcc, 0, v3, vcc
	global_load_dwordx2 v[106:107], v[2:3], off
	global_load_dwordx2 v[108:109], v[2:3], off offset:256
	global_load_dwordx2 v[110:111], v[2:3], off offset:512
	global_load_dwordx2 v[112:113], v[2:3], off offset:768
	global_load_dwordx2 v[114:115], v[2:3], off offset:1024
	global_load_dwordx2 v[116:117], v[2:3], off offset:1280
	global_load_dwordx2 v[118:119], v[2:3], off offset:1536
	global_load_dwordx2 v[120:121], v[2:3], off offset:1792
	v_lshlrev_b32_e32 v123, 5, v1
	global_load_dwordx4 v[6:9], v123, s[8:9]
	global_load_dwordx4 v[2:5], v123, s[10:11]
	global_load_dwordx4 v[14:17], v123, s[8:9] offset:16
	global_load_dwordx4 v[10:13], v123, s[10:11] offset:16
	s_movk_i32 s8, 0x110
	s_waitcnt vmcnt(36)
	ds_write_b128 v122, v[22:25] offset:34816
	ds_write_b128 v122, v[26:29] offset:38976
	ds_write_b128 v122, v[30:33] offset:43136
	ds_write_b128 v122, v[34:37] offset:47296
	ds_write_b128 v122, v[38:41] offset:51456
	ds_write_b128 v122, v[42:45] offset:55616
	s_waitcnt vmcnt(36)
	ds_write_b128 v122, v[46:49] offset:59776
	s_waitcnt vmcnt(36)
	ds_write_b128 v122, v[50:53] offset:63936
	v_mul_u32_u24_e32 v22, 0x410, v56
	v_lshlrev_b32_e32 v23, 2, v57
	v_and_b32_e32 v24, 32, v0
	v_add3_u32 v38, v22, v23, v24
	s_waitcnt lgkmcnt(0)
	ds_read_b128 v[22:25], v38 offset:34832
	ds_read_b128 v[26:29], v38 offset:34816
	ds_read_b128 v[30:33], v38 offset:34880
	ds_read_b128 v[34:37], v38 offset:34896
	s_waitcnt lgkmcnt(3)
	v_cvt_pk_f16_f32 v25, v24, v25
	v_cvt_pk_f16_f32 v24, v22, v23
	s_waitcnt lgkmcnt(2)
	v_cvt_pk_f16_f32 v23, v28, v29
	v_cvt_pk_f16_f32 v22, v26, v27
	s_waitcnt vmcnt(28)
	v_cvt_pk_f16_f32 v29, v70, v72
	v_cvt_pk_f16_f32 v28, v66, v68
	v_cvt_pk_f16_f32 v27, v62, v64
	v_cvt_pk_f16_f32 v26, v58, v60
	v_lshlrev_b32_e32 v19, 2, v55
	s_nop 0
	v_mfma_f32_32x32x16_f16 a[0:15], v[22:25], v[26:29], 0
	s_waitcnt vmcnt(28)
	v_cvt_pk_f16_f32 v29, v71, v73
	v_cvt_pk_f16_f32 v28, v67, v69
	v_cvt_pk_f16_f32 v27, v63, v65
	v_cvt_pk_f16_f32 v26, v59, v61
	s_nop 1
	v_mfma_f32_32x32x16_f16 a[16:31], v[22:25], v[26:29], 0
	s_waitcnt lgkmcnt(0)
	v_cvt_pk_f16_f32 v25, v36, v37
	v_cvt_pk_f16_f32 v24, v34, v35
	v_cvt_pk_f16_f32 v23, v32, v33
	v_cvt_pk_f16_f32 v22, v30, v31
	ds_read_b128 v[30:33], v38 offset:34944
	ds_read_b128 v[34:37], v38 offset:34960
	s_waitcnt vmcnt(20)
	v_cvt_pk_f16_f32 v29, v86, v88
	v_cvt_pk_f16_f32 v28, v82, v84
	v_cvt_pk_f16_f32 v27, v78, v80
	s_waitcnt vmcnt(20)
	v_cvt_pk_f16_f32 v26, v74, v76
	s_nop 1
	v_mfma_f32_32x32x16_f16 a[0:15], v[22:25], v[26:29], a[0:15]
	v_cvt_pk_f16_f32 v29, v87, v89
	v_cvt_pk_f16_f32 v28, v83, v85
	v_cvt_pk_f16_f32 v27, v79, v81
	v_cvt_pk_f16_f32 v26, v75, v77
	s_nop 1
	v_mfma_f32_32x32x16_f16 a[16:31], v[22:25], v[26:29], a[16:31]
	s_waitcnt lgkmcnt(0)
	v_cvt_pk_f16_f32 v25, v36, v37
	v_cvt_pk_f16_f32 v24, v34, v35
	v_cvt_pk_f16_f32 v23, v32, v33
	v_cvt_pk_f16_f32 v22, v30, v31
	ds_read_b128 v[30:33], v38 offset:35008
	ds_read_b128 v[34:37], v38 offset:35024
	s_waitcnt vmcnt(12)
	v_cvt_pk_f16_f32 v29, v102, v104
	v_cvt_pk_f16_f32 v28, v98, v100
	v_cvt_pk_f16_f32 v27, v94, v96
	v_cvt_pk_f16_f32 v26, v90, v92
	s_nop 1
	v_mfma_f32_32x32x16_f16 a[0:15], v[22:25], v[26:29], a[0:15]
	s_waitcnt vmcnt(12)
	v_cvt_pk_f16_f32 v29, v103, v105
	v_cvt_pk_f16_f32 v28, v99, v101
	v_cvt_pk_f16_f32 v27, v95, v97
	v_cvt_pk_f16_f32 v26, v91, v93
	s_nop 1
	v_mfma_f32_32x32x16_f16 a[16:31], v[22:25], v[26:29], a[16:31]
	s_waitcnt lgkmcnt(0)
	v_cvt_pk_f16_f32 v25, v36, v37
	v_cvt_pk_f16_f32 v24, v34, v35
	v_cvt_pk_f16_f32 v23, v32, v33
	v_cvt_pk_f16_f32 v22, v30, v31
	s_waitcnt vmcnt(4)
	v_cvt_pk_f16_f32 v29, v118, v120
	v_cvt_pk_f16_f32 v28, v114, v116
	v_cvt_pk_f16_f32 v27, v110, v112
	v_cvt_pk_f16_f32 v26, v106, v108
	s_nop 1
	v_mfma_f32_32x32x16_f16 a[0:15], v[22:25], v[26:29], a[0:15]
	s_waitcnt vmcnt(4)
	v_cvt_pk_f16_f32 v29, v119, v121
	v_cvt_pk_f16_f32 v28, v115, v117
	v_cvt_pk_f16_f32 v27, v111, v113
	v_cvt_pk_f16_f32 v26, v107, v109
	s_nop 1
	v_mfma_f32_32x32x16_f16 a[16:31], v[22:25], v[26:29], a[16:31]
	v_lshl_or_b32 v22, v54, 5, v19
	v_mul_u32_u24_e32 v22, 0x44, v22
	v_lshl_add_u32 v22, v22, 2, v18
	v_add_u32_e32 v22, v22, v18
	v_add_u32_e32 v23, 0x880, v22
	v_add_u32_e32 v24, 0x1100, v22
	v_add_u32_e32 v25, 0x1980, v22
	s_nop 5
	ds_write2_b32 v22, a0, a16 offset1:1
	ds_write2_b32 v22, a1, a17 offset0:68 offset1:69
	ds_write2_b32 v22, a2, a18 offset0:136 offset1:137
	ds_write2_b32 v22, a3, a19 offset0:204 offset1:205
	ds_write2_b32 v23, a4, a20 offset1:1
	ds_write2_b32 v23, a5, a21 offset0:68 offset1:69
	ds_write2_b32 v23, a6, a22 offset0:136 offset1:137
	ds_write2_b32 v23, a7, a23 offset0:204 offset1:205
	ds_write2_b32 v24, a8, a24 offset1:1
	ds_write2_b32 v24, a9, a25 offset0:68 offset1:69
	ds_write2_b32 v24, a10, a26 offset0:136 offset1:137
	ds_write2_b32 v24, a11, a27 offset0:204 offset1:205
	ds_write2_b32 v25, a12, a28 offset1:1
	ds_write2_b32 v25, a13, a29 offset0:68 offset1:69
	ds_write2_b32 v25, a14, a30 offset0:136 offset1:137
	ds_write2_b32 v25, a15, a31 offset0:204 offset1:205
	v_lshrrev_b32_e32 v22, 3, v0
	v_mad_u32_u24 v23, v22, s8, v123
	s_waitcnt lgkmcnt(0)
	s_barrier
	ds_read_b128 v[24:27], v23
	ds_read_b128 v[28:31], v23 offset:16
	ds_read_b128 v[32:35], v23 offset:8704
	s_waitcnt lgkmcnt(2)
	v_pk_add_f32 v[36:37], v[26:27], 0 op_sel_hi:[1,0]
	v_pk_add_f32 v[38:39], v[24:25], 0 op_sel_hi:[1,0]
	ds_read_b128 v[24:27], v23 offset:8720
	s_waitcnt lgkmcnt(2)
	v_pk_add_f32 v[40:41], v[30:31], 0 op_sel_hi:[1,0]
	v_pk_add_f32 v[42:43], v[28:29], 0 op_sel_hi:[1,0]
	ds_read_b128 v[28:31], v23 offset:17408
	s_waitcnt lgkmcnt(2)
	v_pk_add_f32 v[34:35], v[36:37], v[34:35]
	v_pk_add_f32 v[36:37], v[38:39], v[32:33]
	s_waitcnt lgkmcnt(1)
	v_pk_add_f32 v[38:39], v[40:41], v[26:27]
	v_pk_add_f32 v[40:41], v[42:43], v[24:25]
	ds_read_b128 v[24:27], v23 offset:17424
	s_waitcnt lgkmcnt(1)
	v_pk_add_f32 v[42:43], v[34:35], v[30:31]
	ds_read_b128 v[30:33], v23 offset:26112
	v_pk_add_f32 v[28:29], v[36:37], v[28:29]
	ds_read_b128 v[34:37], v23 offset:26128
	s_waitcnt lgkmcnt(2)
	v_pk_add_f32 v[40:41], v[40:41], v[24:25]
	v_pk_add_f32 v[38:39], v[38:39], v[26:27]
	s_waitcnt lgkmcnt(1)
	v_pk_add_f32 v[24:25], v[28:29], v[30:31]
	v_pk_add_f32 v[26:27], v[42:43], v[32:33]
	s_waitcnt lgkmcnt(0)
	v_pk_add_f32 v[28:29], v[40:41], v[34:35]
	v_pk_add_f32 v[30:31], v[38:39], v[36:37]
	s_waitcnt vmcnt(0)
	v_mul_f32_e32 v10, v28, v10
	v_fmac_f32_e32 v10, v24, v2
	v_mul_f32_e32 v14, v28, v14
	v_add_f32_e32 v2, 0, v10
	v_mul_f32_e32 v10, v29, v15
	v_fmac_f32_e32 v14, v24, v6
	v_fmac_f32_e32 v10, v25, v7
	v_mul_f32_e32 v7, v29, v11
	v_add_f32_e32 v6, 0, v14
	v_fmac_f32_e32 v7, v25, v3
	v_mul_f32_e32 v3, v30, v16
	v_add_f32_e32 v6, v6, v10
	v_fmac_f32_e32 v3, v26, v8
	v_add_f32_e32 v3, v6, v3
	v_mul_f32_e32 v6, v30, v12
	v_fmac_f32_e32 v6, v26, v4
	v_mul_f32_e32 v4, v31, v17
	v_fmac_f32_e32 v4, v27, v9
	v_add_f32_e32 v2, v2, v7
	v_add_f32_e32 v3, v3, v4
	v_mul_f32_e32 v4, v31, v13
	v_add_f32_e32 v2, v2, v6
	v_fmac_f32_e32 v4, v27, v5
	v_add_f32_e32 v2, v2, v4
	ds_write_b128 v23, v[24:27]
	ds_write_b128 v23, v[28:31] offset:16
	s_nop 1
	v_add_f32_dpp v3, v3, v3 quad_perm:[1,0,3,2] row_mask:0xf bank_mask:0xf
	v_add_f32_dpp v6, v2, v2 quad_perm:[1,0,3,2] row_mask:0xf bank_mask:0xf
	s_nop 1
	v_add_f32_dpp v3, v3, v3 quad_perm:[2,3,0,1] row_mask:0xf bank_mask:0xf
	v_add_f32_dpp v6, v6, v6 quad_perm:[2,3,0,1] row_mask:0xf bank_mask:0xf
	s_nop 1
	v_add_f32_dpp v2, v3, v3 row_half_mirror row_mask:0xf bank_mask:0xf
	v_add_f32_dpp v3, v6, v6 row_half_mirror row_mask:0xf bank_mask:0xf
	v_cmp_eq_u32_e32 vcc, 0, v1
	s_and_saveexec_b64 s[6:7], vcc
	s_cbranch_execz .LBB0_2
	v_mul_f32_e32 v4, 0x3f7d70a4, v3
	v_mul_f32_e32 v4, 0x3fb8aa3b, v4
	v_mul_f32_e32 v3, 0x3c23d70a, v3
	v_exp_f32_e32 v4, v4
	v_mul_f32_e32 v3, 0x3fb8aa3b, v3
	v_exp_f32_e32 v3, v3
	v_lshlrev_b32_e32 v5, 2, v22
	v_or_b32_e32 v6, 0x10a80, v5
	v_mul_f32_e32 v2, 0xbf7d70a4, v2
	ds_write_b32 v6, v4
	v_or_b32_e32 v4, 0x10a00, v5
	v_mul_f32_e32 v2, 0x3fb8aa3b, v2
	ds_write_b32 v4, v3
	v_exp_f32_e32 v4, v2
	v_add_u32_e32 v2, s3, v22
	v_ashrrev_i32_e32 v3, 31, v2
	v_lshl_add_u64 v[2:3], v[2:3], 2, s[18:19]
	global_store_dword v[2:3], v4, off sc1
